# tail conversion v5: 4 items per idle CU at MoE GEMM2 tail sites and 2 at neighbourhood-attention site (4992 items hidden) + attention wave priority + DMA rebalance
# baseline (speedup 1.0000x reference)
.LBB0_55:
	s_cmp_lg_u32 s99, 0
	s_cbranch_scc1 .Ltc_itemdone
	v_readlane_b32 s2, v254, 0
	v_readlane_b32 s3, v254, 1
	s_load_dword s0, s[2:3], 0xe8
	s_add_i32 s14, s14, s15
	s_add_i32 s16, s16, s17
	s_add_i32 s10, s10, s18
	s_waitcnt lgkmcnt(0)
	s_add_i32 s22, s22, s0
	s_cmp_lt_i32 s22, 0x1080
	s_cbranch_scc1 .Ltc_noskip
	s_cmp_ge_i32 s22, 0x2000
	s_cbranch_scc1 .Ltc_noskip
	s_and_b32 s22, s22, 0xff
	s_addk_i32 s22, 0x2000
	s_lshl_b32 s14, s22, 5
	s_lshl_b32 s16, s22, 4
	s_lshl_b32 s10, s22, 9

.Ltc_next:
	s_cmp_ge_u32 s100, 0x1380
	s_cbranch_scc1 .Ltc_alldone
	s_movk_i32 s0, 0x1c80
	s_cmp_lt_u32 s100, 0xf80
	s_cselect_b32 s22, 0x1080, s0
	s_add_i32 s22, s22, s100
	v_mbcnt_lo_u32_b32 v0, -1, 0
	v_mbcnt_hi_u32_b32 v0, -1, v0
	s_and_b32 s0, s94, 0xffffffc0
	s_nop 0
	v_ashrrev_i32_e32 v1, 31, v0
	v_add_u32_e32 v2, s0, v0
	s_movk_i32 s0, 0x44
	v_lshlrev_b32_e32 v5, 7, v0
	v_mul_lo_u32 v4, v0, s0
	v_mul_lo_u32 v12, v2, s0
	v_lshrrev_b32_e32 v3, 1, v2
	v_and_b32_e32 v5, 0x80, v5
	s_movk_i32 s0, 0x7f
	v_and_or_b32 v3, v3, s0, v5
	s_lshl_b32 s6, s95, 3
	s_add_u32 s7, s88, 0x22000000
	s_addc_u32 s11, s89, 0
	v_add_u32_e32 v4, 0, v4
	s_add_u32 s12, s88, 0x2000000
	v_add_u32_e32 v4, s6, v4
	s_mov_b32 s1, 0
	s_addc_u32 s13, s89, 0
	s_lshl_b32 s14, s22, 5
	s_lshl_b32 s16, s22, 4
	s_lshl_b32 s10, s22, 9
	s_mov_b32 s19, 0xc3e00000
	s_movk_i32 s20, 0xff
	v_add_u32_e32 v5, 0x1100, v4
	v_add_u32_e32 v6, 0x2200, v4
	v_add_u32_e32 v7, 0x3300, v4
	v_add_u32_e32 v8, 0x4400, v4
	v_add_u32_e32 v9, 0x5500, v4
	v_add_u32_e32 v10, 0x6600, v4
	v_add_u32_e32 v11, 0x7700, v4
	v_add_u32_e32 v12, 0, v12
	s_movk_i32 s21, 0xff00
	v_mov_b32_e32 v13, 0x43e00000
	v_mov_b32_e32 v14, 8
	s_branch .LBB0_56

.LBB0_668:
	s_cmp_lt_u32 s96, 144
	s_cbranch_scc1 .Ltc_skip_4
	v_writelane_b32 v200, s0, 0
	s_nop 1
	v_writelane_b32 v200, s1, 1
	s_nop 1
	v_writelane_b32 v200, s2, 2
	s_nop 1
	v_writelane_b32 v200, s3, 3
	s_nop 1
	v_writelane_b32 v200, s4, 4
	s_nop 1
	v_writelane_b32 v200, s5, 5
	s_nop 1
	v_writelane_b32 v200, s6, 6
	s_nop 1
	v_writelane_b32 v200, s7, 7
	s_nop 1
	v_writelane_b32 v200, s10, 8
	s_nop 1
	v_writelane_b32 v200, s11, 9
	s_nop 1
	v_writelane_b32 v200, s12, 10
	s_nop 1
	v_writelane_b32 v200, s13, 11
	s_nop 1
	v_writelane_b32 v200, s14, 12
	s_nop 1
	v_writelane_b32 v200, s15, 13
	s_nop 1
	v_writelane_b32 v200, s16, 14
	s_nop 1
	v_writelane_b32 v200, s17, 15
	s_nop 1
	v_writelane_b32 v200, s18, 16
	s_nop 1
	v_writelane_b32 v200, s19, 17
	s_nop 1
	v_writelane_b32 v200, s20, 18
	s_nop 1
	v_writelane_b32 v200, s21, 19
	s_nop 1
	v_writelane_b32 v200, s22, 20
	s_nop 1
	v_writelane_b32 v200, s23, 21
	s_nop 1
	v_writelane_b32 v200, s24, 22
	s_nop 1
	v_writelane_b32 v200, s25, 23
	s_nop 1
	v_writelane_b32 v200, s36, 24
	s_nop 1
	v_writelane_b32 v200, s37, 25
	s_nop 1
	v_writelane_b32 v200, s38, 26
	s_nop 1
	v_writelane_b32 v200, s39, 27
	s_nop 1
	v_writelane_b32 v200, s40, 28
	s_nop 1
	v_writelane_b32 v200, s41, 29
	s_nop 1
	v_writelane_b32 v200, s42, 30
	s_nop 1
	v_writelane_b32 v200, s43, 31
	s_nop 1
	v_writelane_b32 v200, s44, 32
	s_nop 1
	v_writelane_b32 v200, s45, 33
	s_nop 1
	v_writelane_b32 v200, s46, 34
	s_nop 1
	v_writelane_b32 v200, s47, 35
	s_nop 1
	v_writelane_b32 v200, s48, 36
	s_nop 1
	v_writelane_b32 v200, s49, 37
	s_nop 1
	v_writelane_b32 v200, s50, 38
	s_nop 1
	v_writelane_b32 v200, s51, 39
	s_nop 1
	s_mov_b32 s99, 4
	s_mov_b32 s98, 4
	s_mov_b32 s101, 112
	s_add_i32 s100, s96, 944
	s_branch .Ltc_next

.LBB0_807:
	s_cmp_lt_u32 s96, 48
	s_cbranch_scc1 .Ltc_skip_5
	v_writelane_b32 v200, s0, 0
	s_nop 1
	v_writelane_b32 v200, s1, 1
	s_nop 1
	v_writelane_b32 v200, s2, 2
	s_nop 1
	v_writelane_b32 v200, s3, 3
	s_nop 1
	v_writelane_b32 v200, s4, 4
	s_nop 1
	v_writelane_b32 v200, s5, 5
	s_nop 1
	v_writelane_b32 v200, s6, 6
	s_nop 1
	v_writelane_b32 v200, s7, 7
	s_nop 1
	v_writelane_b32 v200, s10, 8
	s_nop 1
	v_writelane_b32 v200, s11, 9
	s_nop 1
	v_writelane_b32 v200, s12, 10
	s_nop 1
	v_writelane_b32 v200, s13, 11
	s_nop 1
	v_writelane_b32 v200, s14, 12
	s_nop 1
	v_writelane_b32 v200, s15, 13
	s_nop 1
	v_writelane_b32 v200, s16, 14
	s_nop 1
	v_writelane_b32 v200, s17, 15
	s_nop 1
	v_writelane_b32 v200, s18, 16
	s_nop 1
	v_writelane_b32 v200, s19, 17
	s_nop 1
	v_writelane_b32 v200, s20, 18
	s_nop 1
	v_writelane_b32 v200, s21, 19
	s_nop 1
	v_writelane_b32 v200, s22, 20
	s_nop 1
	v_writelane_b32 v200, s23, 21
	s_nop 1
	v_writelane_b32 v200, s24, 22
	s_nop 1
	v_writelane_b32 v200, s25, 23
	s_nop 1
	v_writelane_b32 v200, s36, 24
	s_nop 1
	v_writelane_b32 v200, s37, 25
	s_nop 1
	v_writelane_b32 v200, s38, 26
	s_nop 1
	v_writelane_b32 v200, s39, 27
	s_nop 1
	v_writelane_b32 v200, s40, 28
	s_nop 1
	v_writelane_b32 v200, s41, 29
	s_nop 1
	v_writelane_b32 v200, s42, 30
	s_nop 1
	v_writelane_b32 v200, s43, 31
	s_nop 1
	v_writelane_b32 v200, s44, 32
	s_nop 1
	v_writelane_b32 v200, s45, 33
	s_nop 1
	v_writelane_b32 v200, s46, 34
	s_nop 1
	v_writelane_b32 v200, s47, 35
	s_nop 1
	v_writelane_b32 v200, s48, 36
	s_nop 1
	v_writelane_b32 v200, s49, 37
	s_nop 1
	v_writelane_b32 v200, s50, 38
	s_nop 1
	v_writelane_b32 v200, s51, 39
	s_nop 1
	s_mov_b32 s99, 5
	s_mov_b32 s98, 2
	s_mov_b32 s101, 208
	s_add_i32 s100, s96, 1488
	s_branch .Ltc_next

.LBB0_1052:
	s_cmp_lt_u32 s96, 32
	s_cbranch_scc1 .Ltc_skip_6
	v_writelane_b32 v200, s0, 0
	s_nop 1
	v_writelane_b32 v200, s1, 1
	s_nop 1
	v_writelane_b32 v200, s2, 2
	s_nop 1
	v_writelane_b32 v200, s3, 3
	s_nop 1
	v_writelane_b32 v200, s4, 4
	s_nop 1
	v_writelane_b32 v200, s5, 5
	s_nop 1
	v_writelane_b32 v200, s6, 6
	s_nop 1
	v_writelane_b32 v200, s7, 7
	s_nop 1
	v_writelane_b32 v200, s10, 8
	s_nop 1
	v_writelane_b32 v200, s11, 9
	s_nop 1
	v_writelane_b32 v200, s12, 10
	s_nop 1
	v_writelane_b32 v200, s13, 11
	s_nop 1
	v_writelane_b32 v200, s14, 12
	s_nop 1
	v_writelane_b32 v200, s15, 13
	s_nop 1
	v_writelane_b32 v200, s16, 14
	s_nop 1
	v_writelane_b32 v200, s17, 15
	s_nop 1
	v_writelane_b32 v200, s18, 16
	s_nop 1
	v_writelane_b32 v200, s19, 17
	s_nop 1
	v_writelane_b32 v200, s20, 18
	s_nop 1
	v_writelane_b32 v200, s21, 19
	s_nop 1
	v_writelane_b32 v200, s22, 20
	s_nop 1
	v_writelane_b32 v200, s23, 21
	s_nop 1
	v_writelane_b32 v200, s24, 22
	s_nop 1
	v_writelane_b32 v200, s25, 23
	s_nop 1
	v_writelane_b32 v200, s36, 24
	s_nop 1
	v_writelane_b32 v200, s37, 25
	s_nop 1
	v_writelane_b32 v200, s38, 26
	s_nop 1
	v_writelane_b32 v200, s39, 27
	s_nop 1
	v_writelane_b32 v200, s40, 28
	s_nop 1
	v_writelane_b32 v200, s41, 29
	s_nop 1
	v_writelane_b32 v200, s42, 30
	s_nop 1
	v_writelane_b32 v200, s43, 31
	s_nop 1
	v_writelane_b32 v200, s44, 32
	s_nop 1
	v_writelane_b32 v200, s45, 33
	s_nop 1
	v_writelane_b32 v200, s46, 34
	s_nop 1
	v_writelane_b32 v200, s47, 35
	s_nop 1
	v_writelane_b32 v200, s48, 36
	s_nop 1
	v_writelane_b32 v200, s49, 37
	s_nop 1
	v_writelane_b32 v200, s50, 38
	s_nop 1
	v_writelane_b32 v200, s51, 39
	s_nop 1
	s_mov_b32 s99, 6
	s_mov_b32 s98, 2
	s_mov_b32 s101, 224
	s_add_i32 s100, s96, 1920
	s_branch .Ltc_next

.LBB0_1361:
	s_cmp_lt_u32 s96, 144
	s_cbranch_scc1 .Ltc_skip_7
	v_writelane_b32 v200, s0, 0
	s_nop 1
	v_writelane_b32 v200, s1, 1
	s_nop 1
	v_writelane_b32 v200, s2, 2
	s_nop 1
	v_writelane_b32 v200, s3, 3
	s_nop 1
	v_writelane_b32 v200, s4, 4
	s_nop 1
	v_writelane_b32 v200, s5, 5
	s_nop 1
	v_writelane_b32 v200, s6, 6
	s_nop 1
	v_writelane_b32 v200, s7, 7
	s_nop 1
	v_writelane_b32 v200, s10, 8
	s_nop 1
	v_writelane_b32 v200, s11, 9
	s_nop 1
	v_writelane_b32 v200, s12, 10
	s_nop 1
	v_writelane_b32 v200, s13, 11
	s_nop 1
	v_writelane_b32 v200, s14, 12
	s_nop 1
	v_writelane_b32 v200, s15, 13
	s_nop 1
	v_writelane_b32 v200, s16, 14
	s_nop 1
	v_writelane_b32 v200, s17, 15
	s_nop 1
	v_writelane_b32 v200, s18, 16
	s_nop 1
	v_writelane_b32 v200, s19, 17
	s_nop 1
	v_writelane_b32 v200, s20, 18
	s_nop 1
	v_writelane_b32 v200, s21, 19
	s_nop 1
	v_writelane_b32 v200, s22, 20
	s_nop 1
	v_writelane_b32 v200, s23, 21
	s_nop 1
	v_writelane_b32 v200, s24, 22
	s_nop 1
	v_writelane_b32 v200, s25, 23
	s_nop 1
	v_writelane_b32 v200, s36, 24
	s_nop 1
	v_writelane_b32 v200, s37, 25
	s_nop 1
	v_writelane_b32 v200, s38, 26
	s_nop 1
	v_writelane_b32 v200, s39, 27
	s_nop 1
	v_writelane_b32 v200, s40, 28
	s_nop 1
	v_writelane_b32 v200, s41, 29
	s_nop 1
	v_writelane_b32 v200, s42, 30
	s_nop 1
	v_writelane_b32 v200, s43, 31
	s_nop 1
	v_writelane_b32 v200, s44, 32
	s_nop 1
	v_writelane_b32 v200, s45, 33
	s_nop 1
	v_writelane_b32 v200, s46, 34
	s_nop 1
	v_writelane_b32 v200, s47, 35
	s_nop 1
	v_writelane_b32 v200, s48, 36
	s_nop 1
	v_writelane_b32 v200, s49, 37
	s_nop 1
	v_writelane_b32 v200, s50, 38
	s_nop 1
	v_writelane_b32 v200, s51, 39
	s_nop 1
	s_mov_b32 s99, 7
	s_mov_b32 s98, 4
	s_mov_b32 s101, 112
	s_add_i32 s100, s96, 2256
	s_branch .Ltc_s1_back

.LBB0_1495:
	s_cmp_lt_u32 s96, 48
	s_cbranch_scc1 .Ltc_skip_8
	v_writelane_b32 v200, s0, 0
	s_nop 1
	v_writelane_b32 v200, s1, 1
	s_nop 1
	v_writelane_b32 v200, s2, 2
	s_nop 1
	v_writelane_b32 v200, s3, 3
	s_nop 1
	v_writelane_b32 v200, s4, 4
	s_nop 1
	v_writelane_b32 v200, s5, 5
	s_nop 1
	v_writelane_b32 v200, s6, 6
	s_nop 1
	v_writelane_b32 v200, s7, 7
	s_nop 1
	v_writelane_b32 v200, s10, 8
	s_nop 1
	v_writelane_b32 v200, s11, 9
	s_nop 1
	v_writelane_b32 v200, s12, 10
	s_nop 1
	v_writelane_b32 v200, s13, 11
	s_nop 1
	v_writelane_b32 v200, s14, 12
	s_nop 1
	v_writelane_b32 v200, s15, 13
	s_nop 1
	v_writelane_b32 v200, s16, 14
	s_nop 1
	v_writelane_b32 v200, s17, 15
	s_nop 1
	v_writelane_b32 v200, s18, 16
	s_nop 1
	v_writelane_b32 v200, s19, 17
	s_nop 1
	v_writelane_b32 v200, s20, 18
	s_nop 1
	v_writelane_b32 v200, s21, 19
	s_nop 1
	v_writelane_b32 v200, s22, 20
	s_nop 1
	v_writelane_b32 v200, s23, 21
	s_nop 1
	v_writelane_b32 v200, s24, 22
	s_nop 1
	v_writelane_b32 v200, s25, 23
	s_nop 1
	v_writelane_b32 v200, s36, 24
	s_nop 1
	v_writelane_b32 v200, s37, 25
	s_nop 1
	v_writelane_b32 v200, s38, 26
	s_nop 1
	v_writelane_b32 v200, s39, 27
	s_nop 1
	v_writelane_b32 v200, s40, 28
	s_nop 1
	v_writelane_b32 v200, s41, 29
	s_nop 1
	v_writelane_b32 v200, s42, 30
	s_nop 1
	v_writelane_b32 v200, s43, 31
	s_nop 1
	v_writelane_b32 v200, s44, 32
	s_nop 1
	v_writelane_b32 v200, s45, 33
	s_nop 1
	v_writelane_b32 v200, s46, 34
	s_nop 1
	v_writelane_b32 v200, s47, 35
	s_nop 1
	v_writelane_b32 v200, s48, 36
	s_nop 1
	v_writelane_b32 v200, s49, 37
	s_nop 1
	v_writelane_b32 v200, s50, 38
	s_nop 1
	v_writelane_b32 v200, s51, 39
	s_nop 1
	s_mov_b32 s99, 8
	s_mov_b32 s98, 2
	s_mov_b32 s101, 208
	s_add_i32 s100, s96, 2800
	s_branch .Ltc_s1_back

.LBB0_1636:
	s_cmp_lt_u32 s96, 64
	s_cbranch_scc1 .Ltc_skip_9
	v_writelane_b32 v200, s0, 0
	s_nop 1
	v_writelane_b32 v200, s1, 1
	s_nop 1
	v_writelane_b32 v200, s2, 2
	s_nop 1
	v_writelane_b32 v200, s3, 3
	s_nop 1
	v_writelane_b32 v200, s4, 4
	s_nop 1
	v_writelane_b32 v200, s5, 5
	s_nop 1
	v_writelane_b32 v200, s6, 6
	s_nop 1
	v_writelane_b32 v200, s7, 7
	s_nop 1
	v_writelane_b32 v200, s10, 8
	s_nop 1
	v_writelane_b32 v200, s11, 9
	s_nop 1
	v_writelane_b32 v200, s12, 10
	s_nop 1
	v_writelane_b32 v200, s13, 11
	s_nop 1
	v_writelane_b32 v200, s14, 12
	s_nop 1
	v_writelane_b32 v200, s15, 13
	s_nop 1
	v_writelane_b32 v200, s16, 14
	s_nop 1
	v_writelane_b32 v200, s17, 15
	s_nop 1
	v_writelane_b32 v200, s18, 16
	s_nop 1
	v_writelane_b32 v200, s19, 17
	s_nop 1
	v_writelane_b32 v200, s20, 18
	s_nop 1
	v_writelane_b32 v200, s21, 19
	s_nop 1
	v_writelane_b32 v200, s22, 20
	s_nop 1
	v_writelane_b32 v200, s23, 21
	s_nop 1
	v_writelane_b32 v200, s24, 22
	s_nop 1
	v_writelane_b32 v200, s25, 23
	s_nop 1
	v_writelane_b32 v200, s36, 24
	s_nop 1
	v_writelane_b32 v200, s37, 25
	s_nop 1
	v_writelane_b32 v200, s38, 26
	s_nop 1
	v_writelane_b32 v200, s39, 27
	s_nop 1
	v_writelane_b32 v200, s40, 28
	s_nop 1
	v_writelane_b32 v200, s41, 29
	s_nop 1
	v_writelane_b32 v200, s42, 30
	s_nop 1
	v_writelane_b32 v200, s43, 31
	s_nop 1
	v_writelane_b32 v200, s44, 32
	s_nop 1
	v_writelane_b32 v200, s45, 33
	s_nop 1
	v_writelane_b32 v200, s46, 34
	s_nop 1
	v_writelane_b32 v200, s47, 35
	s_nop 1
	v_writelane_b32 v200, s48, 36
	s_nop 1
	v_writelane_b32 v200, s49, 37
	s_nop 1
	v_writelane_b32 v200, s50, 38
	s_nop 1
	v_writelane_b32 v200, s51, 39
	s_nop 1
	s_mov_b32 s99, 9
	s_mov_b32 s98, 2
	s_mov_b32 s101, 192
	s_add_i32 s100, s96, 3200
	s_branch .Ltc_s1_back

.LBB0_1711:
	s_cmp_lt_u32 s96, 32
	s_cbranch_scc1 .Ltc_skip_10
	v_writelane_b32 v200, s0, 0
	s_nop 1
	v_writelane_b32 v200, s1, 1
	s_nop 1
	v_writelane_b32 v200, s2, 2
	s_nop 1
	v_writelane_b32 v200, s3, 3
	s_nop 1
	v_writelane_b32 v200, s4, 4
	s_nop 1
	v_writelane_b32 v200, s5, 5
	s_nop 1
	v_writelane_b32 v200, s6, 6
	s_nop 1
	v_writelane_b32 v200, s7, 7
	s_nop 1
	v_writelane_b32 v200, s10, 8
	s_nop 1
	v_writelane_b32 v200, s11, 9
	s_nop 1
	v_writelane_b32 v200, s12, 10
	s_nop 1
	v_writelane_b32 v200, s13, 11
	s_nop 1
	v_writelane_b32 v200, s14, 12
	s_nop 1
	v_writelane_b32 v200, s15, 13
	s_nop 1
	v_writelane_b32 v200, s16, 14
	s_nop 1
	v_writelane_b32 v200, s17, 15
	s_nop 1
	v_writelane_b32 v200, s18, 16
	s_nop 1
	v_writelane_b32 v200, s19, 17
	s_nop 1
	v_writelane_b32 v200, s20, 18
	s_nop 1
	v_writelane_b32 v200, s21, 19
	s_nop 1
	v_writelane_b32 v200, s22, 20
	s_nop 1
	v_writelane_b32 v200, s23, 21
	s_nop 1
	v_writelane_b32 v200, s24, 22
	s_nop 1
	v_writelane_b32 v200, s25, 23
	s_nop 1
	v_writelane_b32 v200, s36, 24
	s_nop 1
	v_writelane_b32 v200, s37, 25
	s_nop 1
	v_writelane_b32 v200, s38, 26
	s_nop 1
	v_writelane_b32 v200, s39, 27
	s_nop 1
	v_writelane_b32 v200, s40, 28
	s_nop 1
	v_writelane_b32 v200, s41, 29
	s_nop 1
	v_writelane_b32 v200, s42, 30
	s_nop 1
	v_writelane_b32 v200, s43, 31
	s_nop 1
	v_writelane_b32 v200, s44, 32
	s_nop 1
	v_writelane_b32 v200, s45, 33
	s_nop 1
	v_writelane_b32 v200, s46, 34
	s_nop 1
	v_writelane_b32 v200, s47, 35
	s_nop 1
	v_writelane_b32 v200, s48, 36
	s_nop 1
	v_writelane_b32 v200, s49, 37
	s_nop 1
	v_writelane_b32 v200, s50, 38
	s_nop 1
	v_writelane_b32 v200, s51, 39
	s_nop 1
	s_mov_b32 s99, 10
	s_mov_b32 s98, 2
	s_mov_b32 s101, 224
	s_add_i32 s100, s96, 3616
	s_branch .Ltc_s1_back

.LBB0_2020:
	s_cmp_lt_u32 s96, 144
	s_cbranch_scc1 .Ltc_skip_11
	v_writelane_b32 v200, s0, 0
	s_nop 1
	v_writelane_b32 v200, s1, 1
	s_nop 1
	v_writelane_b32 v200, s2, 2
	s_nop 1
	v_writelane_b32 v200, s3, 3
	s_nop 1
	v_writelane_b32 v200, s4, 4
	s_nop 1
	v_writelane_b32 v200, s5, 5
	s_nop 1
	v_writelane_b32 v200, s6, 6
	s_nop 1
	v_writelane_b32 v200, s7, 7
	s_nop 1
	v_writelane_b32 v200, s10, 8
	s_nop 1
	v_writelane_b32 v200, s11, 9
	s_nop 1
	v_writelane_b32 v200, s12, 10
	s_nop 1
	v_writelane_b32 v200, s13, 11
	s_nop 1
	v_writelane_b32 v200, s14, 12
	s_nop 1
	v_writelane_b32 v200, s15, 13
	s_nop 1
	v_writelane_b32 v200, s16, 14
	s_nop 1
	v_writelane_b32 v200, s17, 15
	s_nop 1
	v_writelane_b32 v200, s18, 16
	s_nop 1
	v_writelane_b32 v200, s19, 17
	s_nop 1
	v_writelane_b32 v200, s20, 18
	s_nop 1
	v_writelane_b32 v200, s21, 19
	s_nop 1
	v_writelane_b32 v200, s22, 20
	s_nop 1
	v_writelane_b32 v200, s23, 21
	s_nop 1
	v_writelane_b32 v200, s24, 22
	s_nop 1
	v_writelane_b32 v200, s25, 23
	s_nop 1
	v_writelane_b32 v200, s36, 24
	s_nop 1
	v_writelane_b32 v200, s37, 25
	s_nop 1
	v_writelane_b32 v200, s38, 26
	s_nop 1
	v_writelane_b32 v200, s39, 27
	s_nop 1
	v_writelane_b32 v200, s40, 28
	s_nop 1
	v_writelane_b32 v200, s41, 29
	s_nop 1
	v_writelane_b32 v200, s42, 30
	s_nop 1
	v_writelane_b32 v200, s43, 31
	s_nop 1
	v_writelane_b32 v200, s44, 32
	s_nop 1
	v_writelane_b32 v200, s45, 33
	s_nop 1
	v_writelane_b32 v200, s46, 34
	s_nop 1
	v_writelane_b32 v200, s47, 35
	s_nop 1
	v_writelane_b32 v200, s48, 36
	s_nop 1
	v_writelane_b32 v200, s49, 37
	s_nop 1
	v_writelane_b32 v200, s50, 38
	s_nop 1
	v_writelane_b32 v200, s51, 39
	s_nop 1
	s_mov_b32 s99, 11
	s_mov_b32 s98, 4
	s_mov_b32 s101, 112
	s_add_i32 s100, s96, 3952
	s_branch .Ltc_s2_back

.LBB0_2154:
	s_cmp_lt_u32 s96, 32
	s_cbranch_scc1 .Ltc_skip_12
	v_writelane_b32 v200, s0, 0
	s_nop 1
	v_writelane_b32 v200, s1, 1
	s_nop 1
	v_writelane_b32 v200, s2, 2
	s_nop 1
	v_writelane_b32 v200, s3, 3
	s_nop 1
	v_writelane_b32 v200, s4, 4
	s_nop 1
	v_writelane_b32 v200, s5, 5
	s_nop 1
	v_writelane_b32 v200, s6, 6
	s_nop 1
	v_writelane_b32 v200, s7, 7
	s_nop 1
	v_writelane_b32 v200, s10, 8
	s_nop 1
	v_writelane_b32 v200, s11, 9
	s_nop 1
	v_writelane_b32 v200, s12, 10
	s_nop 1
	v_writelane_b32 v200, s13, 11
	s_nop 1
	v_writelane_b32 v200, s14, 12
	s_nop 1
	v_writelane_b32 v200, s15, 13
	s_nop 1
	v_writelane_b32 v200, s16, 14
	s_nop 1
	v_writelane_b32 v200, s17, 15
	s_nop 1
	v_writelane_b32 v200, s18, 16
	s_nop 1
	v_writelane_b32 v200, s19, 17
	s_nop 1
	v_writelane_b32 v200, s20, 18
	s_nop 1
	v_writelane_b32 v200, s21, 19
	s_nop 1
	v_writelane_b32 v200, s22, 20
	s_nop 1
	v_writelane_b32 v200, s23, 21
	s_nop 1
	v_writelane_b32 v200, s24, 22
	s_nop 1
	v_writelane_b32 v200, s25, 23
	s_nop 1
	v_writelane_b32 v200, s36, 24
	s_nop 1
	v_writelane_b32 v200, s37, 25
	s_nop 1
	v_writelane_b32 v200, s38, 26
	s_nop 1
	v_writelane_b32 v200, s39, 27
	s_nop 1
	v_writelane_b32 v200, s40, 28
	s_nop 1
	v_writelane_b32 v200, s41, 29
	s_nop 1
	v_writelane_b32 v200, s42, 30
	s_nop 1
	v_writelane_b32 v200, s43, 31
	s_nop 1
	v_writelane_b32 v200, s44, 32
	s_nop 1
	v_writelane_b32 v200, s45, 33
	s_nop 1
	v_writelane_b32 v200, s46, 34
	s_nop 1
	v_writelane_b32 v200, s47, 35
	s_nop 1
	v_writelane_b32 v200, s48, 36
	s_nop 1
	v_writelane_b32 v200, s49, 37
	s_nop 1
	v_writelane_b32 v200, s50, 38
	s_nop 1
	v_writelane_b32 v200, s51, 39
	s_nop 1
	s_mov_b32 s99, 12
	s_mov_b32 s98, 2
	s_mov_b32 s101, 224
	s_add_i32 s100, s96, 4512
	s_branch .Ltc_s2_back
